# speedup vs baseline: 1.0100x; 1.0100x over previous
.Lk2_nodred:
	s_or_b64 exec, exec, s[2:3]
	v_lshrrev_b32_e32 v6, 3, v0
	v_and_b32_e32 v7, 7, v0
	v_lshrrev_b32_e32 v8, 8, v0
	v_bfe_u32 v9, v0, 3, 5
	v_lshlrev_b32_e32 v10, 2, v9
	v_lshl_or_b32 v10, v8, 7, v10
	v_add_u32_e32 v10, 0x10800, v10
	v_mul_u32_u24_e32 v11, 0x1080, v8
	v_mul_u32_u24_e32 v12, 0x210, v7
	v_lshlrev_b32_e32 v13, 4, v9
	v_add3_u32 v11, v11, v12, v13
	s_lshl_b32 s4, s18, 6
	v_or_b32_e32 v14, s4, v6
	v_mov_b32_e32 v15, 0
	v_lshlrev_b64 v[16:17], 8, v[14:15]
	v_lshl_add_u64 v[16:17], s[12:13], 0, v[16:17]
	s_lshl_b32 s2, s16, 7
	s_mov_b32 s3, 0
	v_lshl_add_u64 v[16:17], v[16:17], 0, s[2:3]
	v_lshlrev_b32_e32 v14, 4, v7
	v_lshl_add_u64 v[16:17], v[16:17], 0, v[14:15]
	s_waitcnt lgkmcnt(0)
	s_barrier
	ds_read_b32 v50, v10
	ds_read_b32 v51, v10 offset:256
	ds_read_b32 v52, v10 offset:512
	ds_read_b32 v53, v10 offset:768
	ds_read_b32 v54, v10 offset:1024
	ds_read_b32 v55, v10 offset:1280
	ds_read_b32 v56, v10 offset:1536
	ds_read_b32 v57, v10 offset:1792
	ds_read_b128 v[18:21], v11
	ds_read_b128 v[22:25], v11 offset:8448
	ds_read_b128 v[26:29], v11 offset:16896
	ds_read_b128 v[30:33], v11 offset:25344
	ds_read_b128 v[34:37], v11 offset:33792
	ds_read_b128 v[38:41], v11 offset:42240
	ds_read_b128 v[42:45], v11 offset:50688
	s_waitcnt lgkmcnt(13)
	ds_read_b128 v[46:49], v11 offset:59136
	v_add_f32_e32 v2, v50, v51
	s_waitcnt lgkmcnt(13)
	v_add_f32_e32 v2, v2, v52
	s_waitcnt lgkmcnt(12)
	v_add_f32_e32 v2, v2, v53
	s_waitcnt lgkmcnt(11)
	v_add_f32_e32 v2, v2, v54
	s_waitcnt lgkmcnt(10)
	v_add_f32_e32 v2, v2, v55
	s_waitcnt lgkmcnt(9)
	v_add_f32_e32 v2, v2, v56
	s_waitcnt lgkmcnt(8)
	v_add_f32_e32 v2, v2, v57
	v_div_scale_f32 v3, s[2:3], v2, v2, 1.0
	v_rcp_f32_e32 v4, v3
	v_div_scale_f32 v5, vcc, 1.0, v2, 1.0
	v_fma_f32 v6, -v3, v4, 1.0
	v_fmac_f32_e32 v4, v6, v4
	v_mul_f32_e32 v6, v5, v4
	v_fma_f32 v7, -v3, v6, v5
	v_fmac_f32_e32 v6, v7, v4
	v_fma_f32 v3, -v3, v6, v5
	v_div_fmas_f32 v3, v3, v4, v6
	v_div_fixup_f32 v8, v3, v2, 1.0
	s_waitcnt lgkmcnt(6)
	v_pk_add_f32 v[60:61], v[20:21], v[24:25]
	v_pk_add_f32 v[58:59], v[18:19], v[22:23]
	s_waitcnt lgkmcnt(5)
	v_pk_add_f32 v[60:61], v[60:61], v[28:29]
	v_pk_add_f32 v[58:59], v[58:59], v[26:27]
	s_waitcnt lgkmcnt(4)
	v_pk_add_f32 v[60:61], v[60:61], v[32:33]
	v_pk_add_f32 v[58:59], v[58:59], v[30:31]
	s_waitcnt lgkmcnt(3)
	v_pk_add_f32 v[60:61], v[60:61], v[36:37]
	v_pk_add_f32 v[58:59], v[58:59], v[34:35]
	s_waitcnt lgkmcnt(2)
	v_pk_add_f32 v[60:61], v[60:61], v[40:41]
	v_pk_add_f32 v[58:59], v[58:59], v[38:39]
	s_waitcnt lgkmcnt(1)
	v_pk_add_f32 v[60:61], v[60:61], v[44:45]
	v_pk_add_f32 v[58:59], v[58:59], v[42:43]
	s_waitcnt lgkmcnt(0)
	v_pk_add_f32 v[60:61], v[60:61], v[48:49]
	v_pk_add_f32 v[58:59], v[58:59], v[46:47]
	v_pk_mul_f32 v[60:61], v[60:61], v[8:9] op_sel_hi:[1,0]
	v_pk_mul_f32 v[58:59], v[58:59], v[8:9] op_sel_hi:[1,0]
	global_store_dwordx4 v[16:17], v[58:61], off sc1
	s_endpgm
